# carry folded into conv|F tail; conv rows split 4 per wave on the carry workgroups, 16 (layer 0) / 14 (layer 1) on the others
# baseline (speedup 1.0000x reference)
; __device__ __forceinline__ void phase_conv(Frame& F, int l, int nblk) {
;     ...
;     const int nrows = l == 0 ? MT : ML, nwv = nblk * NWAVES, rpw = (nrows + nwv - 1) / nwv, r_lo = (F.vcu * NWAVES + F.wave) * rpw, r_hi = r_lo + rpw < nrows ? r_lo + rpw : nrows;
;     if (r_lo >= r_hi) return;
.LBB0_429:
	s_lshl_b32 s0, s14, 3
	s_abs_i32 s1, s0
	v_cvt_f32_u32_e32 v1, s1
	s_add_i32 s3, s0, 0x47ff
	s_sub_i32 s4, 0xffffb801, s0
	s_xor_b32 s0, s3, s0
	v_rcp_iflag_f32_e32 v1, v1
	s_max_i32 s3, s3, s4
	s_sub_i32 s4, 0, s1
	s_ashr_i32 s2, s13, 6
	v_mul_f32_e32 v1, 0x4f7ffffe, v1
	v_cvt_u32_f32_e32 v1, v1
	s_ashr_i32 s0, s0, 31
	v_readfirstlane_b32 s5, v1
	s_mul_i32 s4, s4, s5
	s_mul_hi_u32 s4, s5, s4
	s_add_i32 s5, s5, s4
	s_mul_hi_u32 s4, s3, s5
	s_mul_i32 s5, s4, s1
	s_sub_i32 s3, s3, s5
	s_add_i32 s6, s4, 1
	s_sub_i32 s5, s3, s1
	s_cmp_ge_u32 s3, s1
	s_cselect_b32 s4, s6, s4
	s_cselect_b32 s3, s5, s3
	s_add_i32 s5, s4, 1
	s_cmp_ge_u32 s3, s1
	s_cselect_b32 s1, s5, s4
	s_xor_b32 s1, s1, s0
	s_sub_i32 s0, s1, s0
	s_lshl_b32 s1, s12, 3
	s_add_i32 s1, s1, s2
	s_cmp_lt_u32 s1, 0x200
	s_cbranch_scc1 .Lcv0_a
	s_mov_b32 s0, 16
	s_sub_i32 s1, s1, 0x200
	s_mul_i32 s2, s0, s1
	s_add_i32 s2, s2, 2048
	s_branch .Lcv0_j
.Lcv0_a:
	s_mov_b32 s0, 4
	s_mul_i32 s2, s0, s1

; __device__ __forceinline__ void phase_conv(Frame& F, int l, int nblk) {
;     ...
;     const int nrows = l == 0 ? MT : ML, nwv = nblk * NWAVES, rpw = (nrows + nwv - 1) / nwv, r_lo = (F.vcu * NWAVES + F.wave) * rpw, r_hi = r_lo + rpw < nrows ? r_lo + rpw : nrows;
;     if (r_lo >= r_hi) return;
.LBB0_1449:
	s_lshl_b32 s0, s14, 3
	s_abs_i32 s1, s0
	v_cvt_f32_u32_e32 v1, s1
	s_add_i32 s3, s0, 0x3fff
	s_sub_i32 s4, 0xffffc001, s0
	s_xor_b32 s0, s3, s0
	v_rcp_iflag_f32_e32 v1, v1
	s_max_i32 s3, s3, s4
	s_sub_i32 s4, 0, s1
	s_ashr_i32 s2, s13, 6
	v_mul_f32_e32 v1, 0x4f7ffffe, v1
	v_cvt_u32_f32_e32 v1, v1
	s_ashr_i32 s0, s0, 31
	v_readfirstlane_b32 s5, v1
	s_mul_i32 s4, s4, s5
	s_mul_hi_u32 s4, s5, s4
	s_add_i32 s5, s5, s4
	s_mul_hi_u32 s4, s3, s5
	s_mul_i32 s5, s4, s1
	s_sub_i32 s3, s3, s5
	s_add_i32 s6, s4, 1
	s_sub_i32 s5, s3, s1
	s_cmp_ge_u32 s3, s1
	s_cselect_b32 s4, s6, s4
	s_cselect_b32 s3, s5, s3
	s_add_i32 s5, s4, 1
	s_cmp_ge_u32 s3, s1
	s_cselect_b32 s1, s5, s4
	s_xor_b32 s1, s1, s0
	s_sub_i32 s0, s1, s0
	s_lshl_b32 s1, s12, 3
	s_add_i32 s1, s1, s2
	s_cmp_lt_u32 s1, 0x200
	s_cbranch_scc1 .Lcv1_a
	s_mov_b32 s0, 14
	s_sub_i32 s1, s1, 0x200
	s_mul_i32 s2, s0, s1
	s_add_i32 s2, s2, 2048
	s_branch .Lcv1_j
